# gather: O(n^2) rank sort of the 128 expert entries replaced by a 16-bucket ballot/mbcnt counting sort on the expert index top bits
# speedup vs baseline: 1.1507x; 1.0092x over previous
.LBB0_1405:
	s_barrier
	s_ashr_i32 s45, s44, 31
	s_lshl_b64 s[0:1], s[44:45], 9
	v_lshl_or_b32 v0, v80, 2, s0
	v_mov_b32_e32 v1, s1
	v_lshl_add_u64 v[2:3], s[46:47], 0, v[0:1]
	v_or_b32_e32 v4, 0x100, v0
	v_mov_b32_e32 v5, s1
	v_lshl_add_u64 v[6:7], s[46:47], 0, v[4:5]
	v_lshl_add_u64 v[0:1], s[48:49], 0, v[0:1]
	v_lshl_add_u64 v[4:5], s[48:49], 0, v[4:5]
	global_load_dword v18, v[2:3], off
	global_load_dword v16, v[6:7], off
	global_load_dword v19, v[0:1], off
	global_load_dword v17, v[4:5], off
	s_lshl_b64 s[0:1], s[44:45], 12
	v_lshl_add_u64 v[100:101], v[84:85], 0, s[0:1]
	global_load_dwordx4 v[0:3], v[100:101], off offset:48
	global_load_dwordx4 v[4:7], v[100:101], off offset:32
	global_load_dwordx4 v[8:11], v[100:101], off offset:16
	global_load_dwordx4 v[12:15], v[100:101], off
	s_waitcnt vmcnt(4)
	v_lshrrev_b32_e32 v20, 10, v18
	v_lshrrev_b32_e32 v21, 10, v16
	v_mov_b32_e32 v24, 0
	v_cmp_eq_u32_e64 s[8:9], v20, 0
	v_cmp_eq_u32_e64 s[14:15], v21, 0
	s_bcnt1_i32_b64 s2, s[8:9]
	s_bcnt1_i32_b64 s4, s[14:15]
	v_mbcnt_lo_u32_b32 v25, s8, v24
	v_mbcnt_hi_u32_b32 v25, s9, v25
	v_add_u32_e32 v24, s2, v24
	v_cndmask_b32_e64 v22, v22, v25, s[8:9]
	v_mbcnt_lo_u32_b32 v26, s14, v24
	v_mbcnt_hi_u32_b32 v26, s15, v26
	v_add_u32_e32 v24, s4, v24
	v_cndmask_b32_e64 v23, v23, v26, s[14:15]
	v_cmp_eq_u32_e64 s[8:9], v20, 1
	v_cmp_eq_u32_e64 s[14:15], v21, 1
	s_bcnt1_i32_b64 s2, s[8:9]
	s_bcnt1_i32_b64 s4, s[14:15]
	v_mbcnt_lo_u32_b32 v25, s8, v24
	v_mbcnt_hi_u32_b32 v25, s9, v25
	v_add_u32_e32 v24, s2, v24
	v_cndmask_b32_e64 v22, v22, v25, s[8:9]
	v_mbcnt_lo_u32_b32 v26, s14, v24
	v_mbcnt_hi_u32_b32 v26, s15, v26
	v_add_u32_e32 v24, s4, v24
	v_cndmask_b32_e64 v23, v23, v26, s[14:15]
	v_cmp_eq_u32_e64 s[8:9], v20, 2
	v_cmp_eq_u32_e64 s[14:15], v21, 2
	s_bcnt1_i32_b64 s2, s[8:9]
	s_bcnt1_i32_b64 s4, s[14:15]
	v_mbcnt_lo_u32_b32 v25, s8, v24
	v_mbcnt_hi_u32_b32 v25, s9, v25
	v_add_u32_e32 v24, s2, v24
	v_cndmask_b32_e64 v22, v22, v25, s[8:9]
	v_mbcnt_lo_u32_b32 v26, s14, v24
	v_mbcnt_hi_u32_b32 v26, s15, v26
	v_add_u32_e32 v24, s4, v24
	v_cndmask_b32_e64 v23, v23, v26, s[14:15]
	v_cmp_eq_u32_e64 s[8:9], v20, 3
	v_cmp_eq_u32_e64 s[14:15], v21, 3
	s_bcnt1_i32_b64 s2, s[8:9]
	s_bcnt1_i32_b64 s4, s[14:15]
	v_mbcnt_lo_u32_b32 v25, s8, v24
	v_mbcnt_hi_u32_b32 v25, s9, v25
	v_add_u32_e32 v24, s2, v24
	v_cndmask_b32_e64 v22, v22, v25, s[8:9]
	v_mbcnt_lo_u32_b32 v26, s14, v24
	v_mbcnt_hi_u32_b32 v26, s15, v26
	v_add_u32_e32 v24, s4, v24
	v_cndmask_b32_e64 v23, v23, v26, s[14:15]
	v_cmp_eq_u32_e64 s[8:9], v20, 4
	v_cmp_eq_u32_e64 s[14:15], v21, 4
	s_bcnt1_i32_b64 s2, s[8:9]
	s_bcnt1_i32_b64 s4, s[14:15]
	v_mbcnt_lo_u32_b32 v25, s8, v24
	v_mbcnt_hi_u32_b32 v25, s9, v25
	v_add_u32_e32 v24, s2, v24
	v_cndmask_b32_e64 v22, v22, v25, s[8:9]
	v_mbcnt_lo_u32_b32 v26, s14, v24
	v_mbcnt_hi_u32_b32 v26, s15, v26
	v_add_u32_e32 v24, s4, v24
	v_cndmask_b32_e64 v23, v23, v26, s[14:15]
	v_cmp_eq_u32_e64 s[8:9], v20, 5
	v_cmp_eq_u32_e64 s[14:15], v21, 5
	s_bcnt1_i32_b64 s2, s[8:9]
	s_bcnt1_i32_b64 s4, s[14:15]
	v_mbcnt_lo_u32_b32 v25, s8, v24
	v_mbcnt_hi_u32_b32 v25, s9, v25
	v_add_u32_e32 v24, s2, v24
	v_cndmask_b32_e64 v22, v22, v25, s[8:9]
	v_mbcnt_lo_u32_b32 v26, s14, v24
	v_mbcnt_hi_u32_b32 v26, s15, v26
	v_add_u32_e32 v24, s4, v24
	v_cndmask_b32_e64 v23, v23, v26, s[14:15]
	v_cmp_eq_u32_e64 s[8:9], v20, 6
	v_cmp_eq_u32_e64 s[14:15], v21, 6
	s_bcnt1_i32_b64 s2, s[8:9]
	s_bcnt1_i32_b64 s4, s[14:15]
	v_mbcnt_lo_u32_b32 v25, s8, v24
	v_mbcnt_hi_u32_b32 v25, s9, v25
	v_add_u32_e32 v24, s2, v24
	v_cndmask_b32_e64 v22, v22, v25, s[8:9]
	v_mbcnt_lo_u32_b32 v26, s14, v24
	v_mbcnt_hi_u32_b32 v26, s15, v26
	v_add_u32_e32 v24, s4, v24
	v_cndmask_b32_e64 v23, v23, v26, s[14:15]
	v_cmp_eq_u32_e64 s[8:9], v20, 7
	v_cmp_eq_u32_e64 s[14:15], v21, 7
	s_bcnt1_i32_b64 s2, s[8:9]
	s_bcnt1_i32_b64 s4, s[14:15]
	v_mbcnt_lo_u32_b32 v25, s8, v24
	v_mbcnt_hi_u32_b32 v25, s9, v25
	v_add_u32_e32 v24, s2, v24
	v_cndmask_b32_e64 v22, v22, v25, s[8:9]
	v_mbcnt_lo_u32_b32 v26, s14, v24
	v_mbcnt_hi_u32_b32 v26, s15, v26
	v_add_u32_e32 v24, s4, v24
	v_cndmask_b32_e64 v23, v23, v26, s[14:15]
	v_cmp_eq_u32_e64 s[8:9], v20, 8
	v_cmp_eq_u32_e64 s[14:15], v21, 8
	s_bcnt1_i32_b64 s2, s[8:9]
	s_bcnt1_i32_b64 s4, s[14:15]
	v_mbcnt_lo_u32_b32 v25, s8, v24
	v_mbcnt_hi_u32_b32 v25, s9, v25
	v_add_u32_e32 v24, s2, v24
	v_cndmask_b32_e64 v22, v22, v25, s[8:9]
	v_mbcnt_lo_u32_b32 v26, s14, v24
	v_mbcnt_hi_u32_b32 v26, s15, v26
	v_add_u32_e32 v24, s4, v24
	v_cndmask_b32_e64 v23, v23, v26, s[14:15]
	v_cmp_eq_u32_e64 s[8:9], v20, 9
	v_cmp_eq_u32_e64 s[14:15], v21, 9
	s_bcnt1_i32_b64 s2, s[8:9]
	s_bcnt1_i32_b64 s4, s[14:15]
	v_mbcnt_lo_u32_b32 v25, s8, v24
	v_mbcnt_hi_u32_b32 v25, s9, v25
	v_add_u32_e32 v24, s2, v24
	v_cndmask_b32_e64 v22, v22, v25, s[8:9]
	v_mbcnt_lo_u32_b32 v26, s14, v24
	v_mbcnt_hi_u32_b32 v26, s15, v26
	v_add_u32_e32 v24, s4, v24
	v_cndmask_b32_e64 v23, v23, v26, s[14:15]
	v_cmp_eq_u32_e64 s[8:9], v20, 10
	v_cmp_eq_u32_e64 s[14:15], v21, 10
	s_bcnt1_i32_b64 s2, s[8:9]
	s_bcnt1_i32_b64 s4, s[14:15]
	v_mbcnt_lo_u32_b32 v25, s8, v24
	v_mbcnt_hi_u32_b32 v25, s9, v25
	v_add_u32_e32 v24, s2, v24
	v_cndmask_b32_e64 v22, v22, v25, s[8:9]
	v_mbcnt_lo_u32_b32 v26, s14, v24
	v_mbcnt_hi_u32_b32 v26, s15, v26
	v_add_u32_e32 v24, s4, v24
	v_cndmask_b32_e64 v23, v23, v26, s[14:15]
	v_cmp_eq_u32_e64 s[8:9], v20, 11
	v_cmp_eq_u32_e64 s[14:15], v21, 11
	s_bcnt1_i32_b64 s2, s[8:9]
	s_bcnt1_i32_b64 s4, s[14:15]
	v_mbcnt_lo_u32_b32 v25, s8, v24
	v_mbcnt_hi_u32_b32 v25, s9, v25
	v_add_u32_e32 v24, s2, v24
	v_cndmask_b32_e64 v22, v22, v25, s[8:9]
	v_mbcnt_lo_u32_b32 v26, s14, v24
	v_mbcnt_hi_u32_b32 v26, s15, v26
	v_add_u32_e32 v24, s4, v24
	v_cndmask_b32_e64 v23, v23, v26, s[14:15]
	v_cmp_eq_u32_e64 s[8:9], v20, 12
	v_cmp_eq_u32_e64 s[14:15], v21, 12
	s_bcnt1_i32_b64 s2, s[8:9]
	s_bcnt1_i32_b64 s4, s[14:15]
	v_mbcnt_lo_u32_b32 v25, s8, v24
	v_mbcnt_hi_u32_b32 v25, s9, v25
	v_add_u32_e32 v24, s2, v24
	v_cndmask_b32_e64 v22, v22, v25, s[8:9]
	v_mbcnt_lo_u32_b32 v26, s14, v24
	v_mbcnt_hi_u32_b32 v26, s15, v26
	v_add_u32_e32 v24, s4, v24
	v_cndmask_b32_e64 v23, v23, v26, s[14:15]
	v_cmp_eq_u32_e64 s[8:9], v20, 13
	v_cmp_eq_u32_e64 s[14:15], v21, 13
	s_bcnt1_i32_b64 s2, s[8:9]
	s_bcnt1_i32_b64 s4, s[14:15]
	v_mbcnt_lo_u32_b32 v25, s8, v24
	v_mbcnt_hi_u32_b32 v25, s9, v25
	v_add_u32_e32 v24, s2, v24
	v_cndmask_b32_e64 v22, v22, v25, s[8:9]
	v_mbcnt_lo_u32_b32 v26, s14, v24
	v_mbcnt_hi_u32_b32 v26, s15, v26
	v_add_u32_e32 v24, s4, v24
	v_cndmask_b32_e64 v23, v23, v26, s[14:15]
	v_cmp_eq_u32_e64 s[8:9], v20, 14
	v_cmp_eq_u32_e64 s[14:15], v21, 14
	s_bcnt1_i32_b64 s2, s[8:9]
	s_bcnt1_i32_b64 s4, s[14:15]
	v_mbcnt_lo_u32_b32 v25, s8, v24
	v_mbcnt_hi_u32_b32 v25, s9, v25
	v_add_u32_e32 v24, s2, v24
	v_cndmask_b32_e64 v22, v22, v25, s[8:9]
	v_mbcnt_lo_u32_b32 v26, s14, v24
	v_mbcnt_hi_u32_b32 v26, s15, v26
	v_add_u32_e32 v24, s4, v24
	v_cndmask_b32_e64 v23, v23, v26, s[14:15]
	v_cmp_eq_u32_e64 s[8:9], v20, 15
	v_cmp_eq_u32_e64 s[14:15], v21, 15
	s_bcnt1_i32_b64 s2, s[8:9]
	s_bcnt1_i32_b64 s4, s[14:15]
	v_mbcnt_lo_u32_b32 v25, s8, v24
	v_mbcnt_hi_u32_b32 v25, s9, v25
	v_add_u32_e32 v24, s2, v24
	v_cndmask_b32_e64 v22, v22, v25, s[8:9]
	v_mbcnt_lo_u32_b32 v26, s14, v24
	v_mbcnt_hi_u32_b32 v26, s15, v26
	v_add_u32_e32 v24, s4, v24
	v_cndmask_b32_e64 v23, v23, v26, s[14:15]
	s_waitcnt vmcnt(3)
	v_lshlrev_b32_e32 v126, 16, v0
	v_and_b32_e32 v127, 0xffff0000, v0
	v_lshl_add_u32 v0, v22, 3, s21
	ds_write_b64 v0, v[18:19] offset:1024
	v_lshl_add_u32 v0, v23, 3, s21
	ds_write_b64 v0, v[16:17] offset:1024
	s_waitcnt vmcnt(2)
	v_lshlrev_b32_e32 v118, 16, v4
	v_and_b32_e32 v119, 0xffff0000, v4
	v_mov_b32_e32 v4, s21
	s_waitcnt lgkmcnt(0)
	v_lshlrev_b32_e32 v128, 16, v1
	v_and_b32_e32 v129, 0xffff0000, v1
	v_lshlrev_b32_e32 v130, 16, v2
	v_and_b32_e32 v131, 0xffff0000, v2
	v_lshlrev_b32_e32 v132, 16, v3
	v_and_b32_e32 v133, 0xffff0000, v3
	ds_read2_b64 v[0:3], v4 offset0:128 offset1:129
	v_mov_b32_e32 v96, v81
	v_lshlrev_b32_e32 v120, 16, v5
	v_and_b32_e32 v121, 0xffff0000, v5
	v_lshlrev_b32_e32 v122, 16, v6
	s_waitcnt lgkmcnt(0)
	v_readfirstlane_b32 s74, v0
	s_lshl_b64 s[4:5], s[74:75], 10
	s_add_u32 s8, s4, s93
	s_addc_u32 s9, s5, s20
	s_add_u32 s4, s4, s89
	s_addc_u32 s5, s5, s92
	s_lshl_b64 s[14:15], s[74:75], 4
	s_add_u32 s14, s14, s6
	v_readfirstlane_b32 s74, v2
	v_and_b32_e32 v123, 0xffff0000, v6
	v_lshlrev_b32_e32 v124, 16, v7
	v_and_b32_e32 v125, 0xffff0000, v7
	ds_read2_b64 v[4:7], v4 offset0:130 offset1:131
	s_addc_u32 s15, s15, s88
	v_lshl_add_u64 v[60:61], s[4:5], 0, v[96:97]
	s_lshl_b64 s[4:5], s[74:75], 10
	v_lshl_add_u64 v[48:49], s[8:9], 0, v[96:97]
	s_add_u32 s8, s4, s93
	s_addc_u32 s9, s5, s20
	s_waitcnt vmcnt(1)
	v_lshlrev_b32_e32 v110, 16, v8
	v_and_b32_e32 v111, 0xffff0000, v8
	v_lshlrev_b32_e32 v112, 16, v9
	v_and_b32_e32 v113, 0xffff0000, v9
	v_mov_b32_e32 v8, v83
	v_mov_b32_e32 v9, v97
	s_add_u32 s4, s4, s89
	s_addc_u32 s5, s5, s92
	v_lshl_add_u64 v[134:135], s[14:15], 0, v[8:9]
	s_lshl_b64 s[14:15], s[74:75], 4
	s_add_u32 s14, s14, s6
	s_waitcnt lgkmcnt(0)
	v_readfirstlane_b32 s74, v4
	s_addc_u32 s15, s15, s88
	v_lshl_add_u64 v[56:57], s[4:5], 0, v[96:97]
	s_lshl_b64 s[4:5], s[74:75], 10
	v_lshl_add_u64 v[50:51], s[8:9], 0, v[96:97]
	s_add_u32 s8, s4, s93
	s_addc_u32 s9, s5, s20
	s_add_u32 s4, s4, s89
	v_lshl_add_u64 v[136:137], s[14:15], 0, v[8:9]
	s_addc_u32 s5, s5, s92
	s_lshl_b64 s[14:15], s[74:75], 4
	s_add_u32 s14, s14, s6
	v_readfirstlane_b32 s74, v6
	s_addc_u32 s15, s15, s88
	v_lshl_add_u64 v[52:53], s[4:5], 0, v[96:97]
	s_lshl_b64 s[4:5], s[74:75], 10
	v_lshl_add_u64 v[58:59], s[8:9], 0, v[96:97]
	s_add_u32 s8, s4, s93
	s_addc_u32 s9, s5, s20
	s_add_u32 s4, s4, s89
	v_lshl_add_u64 v[138:139], s[14:15], 0, v[8:9]
	s_addc_u32 s5, s5, s92
	s_lshl_b64 s[14:15], s[74:75], 4
	s_add_u32 s14, s14, s6
	s_addc_u32 s15, s15, s88
	v_mov_b32_e32 v178, 0
	s_waitcnt vmcnt(0)
	v_lshlrev_b32_e32 v102, 16, v12
	v_and_b32_e32 v103, 0xffff0000, v12
	v_lshlrev_b32_e32 v104, 16, v13
	v_and_b32_e32 v105, 0xffff0000, v13
	v_lshlrev_b32_e32 v106, 16, v14
	v_and_b32_e32 v107, 0xffff0000, v14
	v_lshlrev_b32_e32 v108, 16, v15
	v_and_b32_e32 v109, 0xffff0000, v15
	v_lshlrev_b32_e32 v114, 16, v10
	v_and_b32_e32 v115, 0xffff0000, v10
	v_lshlrev_b32_e32 v116, 16, v11
	v_and_b32_e32 v117, 0xffff0000, v11
	v_lshl_add_u64 v[54:55], s[4:5], 0, v[96:97]
	v_lshl_add_u64 v[62:63], s[8:9], 0, v[96:97]
	v_lshl_add_u64 v[140:141], s[14:15], 0, v[8:9]
	s_mov_b32 s4, -2
	s_mov_b32 s5, s83
	v_mov_b32_e32 v179, v178
	v_mov_b32_e32 v184, v178
	v_mov_b32_e32 v185, v178
	v_mov_b32_e32 v182, v178
	v_mov_b32_e32 v183, v178
	v_mov_b32_e32 v180, v178
	v_mov_b32_e32 v181, v178
	v_mov_b32_e32 v176, v178
	v_mov_b32_e32 v177, v178
	v_mov_b32_e32 v174, v178
	v_mov_b32_e32 v175, v178
	v_mov_b32_e32 v160, v178
	v_mov_b32_e32 v161, v178
	v_mov_b32_e32 v158, v178
	v_mov_b32_e32 v159, v178
	v_mov_b32_e32 v156, v178
	v_mov_b32_e32 v157, v178
	v_mov_b32_e32 v154, v178
	v_mov_b32_e32 v155, v178
	v_mov_b32_e32 v152, v178
	v_mov_b32_e32 v153, v178
	v_mov_b32_e32 v150, v178
	v_mov_b32_e32 v151, v178
	v_mov_b32_e32 v148, v178
	v_mov_b32_e32 v149, v178
	v_mov_b32_e32 v146, v178
	v_mov_b32_e32 v147, v178
	v_mov_b32_e32 v144, v178
	v_mov_b32_e32 v145, v178
	v_mov_b32_e32 v142, v178
	v_mov_b32_e32 v143, v178
